# reader-part issue priority extended to the out-proj and moe1 p8 K-loops as well
# baseline (speedup 1.0000x reference)
.LBB0_2136:
	s_add_u32 s18, s16, 0x100
	s_addc_u32 s19, s17, 0
	s_add_i32 s46, 0, 0x10000
	v_add_u32_e32 v2, s46, v149
	ds_read_b128 v[144:147], v2
	ds_read_b128 v[152:155], v2 offset:1024
	ds_read_b128 v[156:159], v2 offset:2048
	ds_read_b128 v[160:163], v2 offset:3072
	s_cmp_eq_u32 s45, 12
	s_cselect_b32 s23, s11, s19
	s_cselect_b32 s22, s10, s18
	s_cselect_b32 s21, s15, s44
	s_cselect_b32 s20, s14, s7
	v_lshl_add_u64 v[196:197], s[16:17], 0, v[140:141]
	s_add_i32 m0, s30, 0xc000
	ds_read_b128 v[164:167], v150
	ds_read_b128 v[168:171], v150 offset:1024
	ds_read_b128 v[172:175], v150 offset:2048
	ds_read_b128 v[176:179], v150 offset:3072
	ds_read_b128 v[180:183], v150 offset:4096
	ds_read_b128 v[184:187], v150 offset:5120
	ds_read_b128 v[188:191], v150 offset:6144
	ds_read_b128 v[192:195], v150 offset:7168
	global_load_lds_dwordx4 v[196:197], off
	v_lshl_add_u64 v[196:197], s[16:17], 0, v[142:143]
	s_add_i32 m0, s30, 0xe000
	s_nop 0
	global_load_lds_dwordx4 v[196:197], off
	s_waitcnt lgkmcnt(8)
	s_barrier
	s_waitcnt lgkmcnt(0)
	s_setprio 0
	s_waitcnt lgkmcnt(0)
	v_mfma_f32_16x16x32_bf16 v[128:131], v[144:147], v[164:167], v[128:131]
	v_mfma_f32_16x16x32_bf16 v[124:127], v[156:159], v[164:167], v[124:127]
	v_mfma_f32_16x16x32_bf16 v[112:115], v[144:147], v[172:175], v[112:115]
	v_mfma_f32_16x16x32_bf16 v[108:111], v[156:159], v[172:175], v[108:111]
	v_mfma_f32_16x16x32_bf16 v[96:99], v[144:147], v[180:183], v[96:99]
	v_mfma_f32_16x16x32_bf16 v[92:95], v[156:159], v[180:183], v[92:95]
	v_mfma_f32_16x16x32_bf16 v[80:83], v[144:147], v[188:191], v[80:83]
	v_mfma_f32_16x16x32_bf16 v[76:79], v[156:159], v[188:191], v[76:79]
	v_mfma_f32_16x16x32_bf16 v[128:131], v[152:155], v[168:171], v[128:131]
	v_mfma_f32_16x16x32_bf16 v[124:127], v[160:163], v[168:171], v[124:127]
	v_mfma_f32_16x16x32_bf16 v[112:115], v[152:155], v[176:179], v[112:115]
	v_mfma_f32_16x16x32_bf16 v[108:111], v[160:163], v[176:179], v[108:111]
	v_mfma_f32_16x16x32_bf16 v[96:99], v[152:155], v[184:187], v[96:99]
	v_mfma_f32_16x16x32_bf16 v[92:95], v[160:163], v[184:187], v[92:95]
	v_mfma_f32_16x16x32_bf16 v[80:83], v[152:155], v[192:195], v[80:83]
	v_mfma_f32_16x16x32_bf16 v[76:79], v[160:163], v[192:195], v[76:79]
	s_setprio 1
	s_barrier
	s_add_i32 s47, 0, 0x14000
	s_add_i32 s16, s46, s29
	v_add_u32_e32 v2, s47, v149
	v_lshl_add_u64 v[212:213], s[20:21], 0, v[136:137]
	s_mov_b32 m0, s16
	ds_read_b128 v[196:199], v2
	ds_read_b128 v[200:203], v2 offset:1024
	ds_read_b128 v[204:207], v2 offset:2048
	ds_read_b128 v[208:211], v2 offset:3072
	global_load_lds_dwordx4 v[212:213], off
	v_lshl_add_u64 v[222:223], s[20:21], 0, v[132:133]
	s_add_i32 m0, s16, 0x2000
	s_nop 0
	global_load_lds_dwordx4 v[222:223], off
	s_barrier
	s_waitcnt lgkmcnt(0)
	s_setprio 0
	s_waitcnt lgkmcnt(0)
	v_mfma_f32_16x16x32_bf16 v[120:123], v[196:199], v[164:167], v[120:123]
	v_mfma_f32_16x16x32_bf16 v[116:119], v[204:207], v[164:167], v[116:119]
	v_mfma_f32_16x16x32_bf16 v[104:107], v[196:199], v[172:175], v[104:107]
	v_mfma_f32_16x16x32_bf16 v[100:103], v[204:207], v[172:175], v[100:103]
	v_mfma_f32_16x16x32_bf16 v[88:91], v[196:199], v[180:183], v[88:91]
	v_mfma_f32_16x16x32_bf16 v[84:87], v[204:207], v[180:183], v[84:87]
	v_mfma_f32_16x16x32_bf16 v[72:75], v[196:199], v[188:191], v[72:75]
	v_mfma_f32_16x16x32_bf16 v[68:71], v[204:207], v[188:191], v[68:71]
	v_mfma_f32_16x16x32_bf16 v[120:123], v[200:203], v[168:171], v[120:123]
	v_mfma_f32_16x16x32_bf16 v[116:119], v[208:211], v[168:171], v[116:119]
	v_mfma_f32_16x16x32_bf16 v[104:107], v[200:203], v[176:179], v[104:107]
	v_mfma_f32_16x16x32_bf16 v[100:103], v[208:211], v[176:179], v[100:103]
	v_mfma_f32_16x16x32_bf16 v[88:91], v[200:203], v[184:187], v[88:91]
	v_mfma_f32_16x16x32_bf16 v[84:87], v[208:211], v[184:187], v[84:87]
	v_mfma_f32_16x16x32_bf16 v[72:75], v[200:203], v[192:195], v[72:75]
	v_mfma_f32_16x16x32_bf16 v[68:71], v[208:211], v[192:195], v[68:71]
	s_setprio 1
	s_mov_b32 m0, s30
	v_lshl_add_u64 v[224:225], s[22:23], 0, v[138:139]
	s_barrier
	ds_read_b128 v[164:167], v150 offset:16384
	ds_read_b128 v[168:171], v150 offset:17408
	ds_read_b128 v[172:175], v150 offset:18432
	ds_read_b128 v[176:179], v150 offset:19456
	ds_read_b128 v[180:183], v150 offset:20480
	ds_read_b128 v[184:187], v150 offset:21504
	ds_read_b128 v[188:191], v150 offset:22528
	ds_read_b128 v[192:195], v150 offset:23552
	global_load_lds_dwordx4 v[224:225], off
	v_lshl_add_u64 v[230:231], s[22:23], 0, v[134:135]
	s_mov_b32 m0, s31
	s_nop 0
	global_load_lds_dwordx4 v[230:231], off
	s_barrier
	s_waitcnt lgkmcnt(0)
	s_setprio 0
	s_waitcnt lgkmcnt(0)
	v_mfma_f32_16x16x32_bf16 v[64:67], v[144:147], v[164:167], v[64:67]
	v_mfma_f32_16x16x32_bf16 v[60:63], v[156:159], v[164:167], v[60:63]
	v_mfma_f32_16x16x32_bf16 v[48:51], v[144:147], v[172:175], v[48:51]
	v_mfma_f32_16x16x32_bf16 v[44:47], v[156:159], v[172:175], v[44:47]
	v_mfma_f32_16x16x32_bf16 v[32:35], v[144:147], v[180:183], v[32:35]
	v_mfma_f32_16x16x32_bf16 v[28:31], v[156:159], v[180:183], v[28:31]
	v_mfma_f32_16x16x32_bf16 v[16:19], v[144:147], v[188:191], v[16:19]
	v_mfma_f32_16x16x32_bf16 v[12:15], v[156:159], v[188:191], v[12:15]
	v_mfma_f32_16x16x32_bf16 v[64:67], v[152:155], v[168:171], v[64:67]
	v_mfma_f32_16x16x32_bf16 v[60:63], v[160:163], v[168:171], v[60:63]
	v_mfma_f32_16x16x32_bf16 v[48:51], v[152:155], v[176:179], v[48:51]
	v_mfma_f32_16x16x32_bf16 v[44:47], v[160:163], v[176:179], v[44:47]
	v_mfma_f32_16x16x32_bf16 v[32:35], v[152:155], v[184:187], v[32:35]
	v_mfma_f32_16x16x32_bf16 v[28:31], v[160:163], v[184:187], v[28:31]
	v_mfma_f32_16x16x32_bf16 v[16:19], v[152:155], v[192:195], v[16:19]
	v_mfma_f32_16x16x32_bf16 v[12:15], v[160:163], v[192:195], v[12:15]
	s_setprio 1
	s_barrier
	s_add_u32 s16, s20, 0x40000
	s_addc_u32 s17, s21, 0
	s_add_i32 s46, s47, s29
	v_lshl_add_u64 v[144:145], s[16:17], 0, v[136:137]
	s_mov_b32 m0, s46
	s_nop 0
	global_load_lds_dwordx4 v[144:145], off
	v_lshl_add_u64 v[144:145], s[16:17], 0, v[132:133]
	s_add_i32 m0, s46, 0x2000
	s_nop 0
	global_load_lds_dwordx4 v[144:145], off
	s_waitcnt vmcnt(6)
	s_barrier
	s_setprio 0
	v_mfma_f32_16x16x32_bf16 v[56:59], v[196:199], v[164:167], v[56:59]
	v_mfma_f32_16x16x32_bf16 v[52:55], v[204:207], v[164:167], v[52:55]
	v_mfma_f32_16x16x32_bf16 v[40:43], v[196:199], v[172:175], v[40:43]
	v_mfma_f32_16x16x32_bf16 v[36:39], v[204:207], v[172:175], v[36:39]
	v_mfma_f32_16x16x32_bf16 v[24:27], v[196:199], v[180:183], v[24:27]
	v_mfma_f32_16x16x32_bf16 v[20:23], v[204:207], v[180:183], v[20:23]
	v_mfma_f32_16x16x32_bf16 v[8:11], v[196:199], v[188:191], v[8:11]
	v_mfma_f32_16x16x32_bf16 v[4:7], v[204:207], v[188:191], v[4:7]
	v_mfma_f32_16x16x32_bf16 v[56:59], v[200:203], v[168:171], v[56:59]
	v_mfma_f32_16x16x32_bf16 v[52:55], v[208:211], v[168:171], v[52:55]
	v_mfma_f32_16x16x32_bf16 v[40:43], v[200:203], v[176:179], v[40:43]
	v_mfma_f32_16x16x32_bf16 v[36:39], v[208:211], v[176:179], v[36:39]
	v_mfma_f32_16x16x32_bf16 v[24:27], v[200:203], v[184:187], v[24:27]
	v_mfma_f32_16x16x32_bf16 v[20:23], v[208:211], v[184:187], v[20:23]
	v_mfma_f32_16x16x32_bf16 v[8:11], v[200:203], v[192:195], v[8:11]
	v_mfma_f32_16x16x32_bf16 v[4:7], v[208:211], v[192:195], v[4:7]
	s_setprio 1
	s_add_i32 s46, 0, 0x18000
	v_add_u32_e32 v2, s46, v149
	s_barrier
	ds_read_b128 v[144:147], v2
	ds_read_b128 v[152:155], v2 offset:1024
	ds_read_b128 v[156:159], v2 offset:2048
	ds_read_b128 v[160:163], v2 offset:3072
	s_add_u32 s16, s22, 0x120000
	s_addc_u32 s17, s23, 0
	s_mov_b32 m0, s34
	v_lshl_add_u64 v[196:197], s[16:17], 0, v[138:139]
	ds_read_b128 v[164:167], v150 offset:32768
	ds_read_b128 v[168:171], v150 offset:33792
	ds_read_b128 v[172:175], v150 offset:34816
	ds_read_b128 v[176:179], v150 offset:35840
	ds_read_b128 v[180:183], v150 offset:36864
	ds_read_b128 v[184:187], v150 offset:37888
	ds_read_b128 v[188:191], v150 offset:38912
	ds_read_b128 v[192:195], v150 offset:39936
	global_load_lds_dwordx4 v[196:197], off
	v_lshl_add_u64 v[196:197], s[16:17], 0, v[134:135]
	s_mov_b32 m0, s35
	s_nop 0
	global_load_lds_dwordx4 v[196:197], off
	s_waitcnt lgkmcnt(8)
	s_barrier
	s_waitcnt lgkmcnt(0)
	s_setprio 0
	s_waitcnt lgkmcnt(0)
	v_mfma_f32_16x16x32_bf16 v[128:131], v[144:147], v[164:167], v[128:131]
	v_mfma_f32_16x16x32_bf16 v[124:127], v[156:159], v[164:167], v[124:127]
	v_mfma_f32_16x16x32_bf16 v[112:115], v[144:147], v[172:175], v[112:115]
	v_mfma_f32_16x16x32_bf16 v[108:111], v[156:159], v[172:175], v[108:111]
	v_mfma_f32_16x16x32_bf16 v[96:99], v[144:147], v[180:183], v[96:99]
	v_mfma_f32_16x16x32_bf16 v[92:95], v[156:159], v[180:183], v[92:95]
	v_mfma_f32_16x16x32_bf16 v[80:83], v[144:147], v[188:191], v[80:83]
	v_mfma_f32_16x16x32_bf16 v[76:79], v[156:159], v[188:191], v[76:79]
	v_mfma_f32_16x16x32_bf16 v[128:131], v[152:155], v[168:171], v[128:131]
	v_mfma_f32_16x16x32_bf16 v[124:127], v[160:163], v[168:171], v[124:127]
	v_mfma_f32_16x16x32_bf16 v[112:115], v[152:155], v[176:179], v[112:115]
	v_mfma_f32_16x16x32_bf16 v[108:111], v[160:163], v[176:179], v[108:111]
	v_mfma_f32_16x16x32_bf16 v[96:99], v[152:155], v[184:187], v[96:99]
	v_mfma_f32_16x16x32_bf16 v[92:95], v[160:163], v[184:187], v[92:95]
	v_mfma_f32_16x16x32_bf16 v[80:83], v[152:155], v[192:195], v[80:83]
	v_mfma_f32_16x16x32_bf16 v[76:79], v[160:163], v[192:195], v[76:79]
	s_setprio 1
	s_barrier
	s_add_i32 s22, 0, 0x1c000
	s_add_i32 s16, s46, s29
	v_add_u32_e32 v2, s22, v149
	v_lshl_add_u64 v[212:213], v[212:213], 0, s[60:61]
	s_mov_b32 m0, s16
	ds_read_b128 v[196:199], v2
	ds_read_b128 v[200:203], v2 offset:1024
	ds_read_b128 v[204:207], v2 offset:2048
	ds_read_b128 v[208:211], v2 offset:3072
	global_load_lds_dwordx4 v[212:213], off
	v_lshl_add_u64 v[212:213], v[222:223], 0, s[60:61]
	s_add_i32 m0, s16, 0x2000
	s_nop 0
	global_load_lds_dwordx4 v[212:213], off
	s_barrier
	s_waitcnt lgkmcnt(0)
	s_setprio 0
	s_waitcnt lgkmcnt(0)
	v_mfma_f32_16x16x32_bf16 v[120:123], v[196:199], v[164:167], v[120:123]
	v_mfma_f32_16x16x32_bf16 v[116:119], v[204:207], v[164:167], v[116:119]
	v_mfma_f32_16x16x32_bf16 v[104:107], v[196:199], v[172:175], v[104:107]
	v_mfma_f32_16x16x32_bf16 v[100:103], v[204:207], v[172:175], v[100:103]
	v_mfma_f32_16x16x32_bf16 v[88:91], v[196:199], v[180:183], v[88:91]
	v_mfma_f32_16x16x32_bf16 v[84:87], v[204:207], v[180:183], v[84:87]
	v_mfma_f32_16x16x32_bf16 v[72:75], v[196:199], v[188:191], v[72:75]
	v_mfma_f32_16x16x32_bf16 v[68:71], v[204:207], v[188:191], v[68:71]
	v_mfma_f32_16x16x32_bf16 v[120:123], v[200:203], v[168:171], v[120:123]
	v_mfma_f32_16x16x32_bf16 v[116:119], v[208:211], v[168:171], v[116:119]
	v_mfma_f32_16x16x32_bf16 v[104:107], v[200:203], v[176:179], v[104:107]
	v_mfma_f32_16x16x32_bf16 v[100:103], v[208:211], v[176:179], v[100:103]
	v_mfma_f32_16x16x32_bf16 v[88:91], v[200:203], v[184:187], v[88:91]
	v_mfma_f32_16x16x32_bf16 v[84:87], v[208:211], v[184:187], v[84:87]
	v_mfma_f32_16x16x32_bf16 v[72:75], v[200:203], v[192:195], v[72:75]
	v_mfma_f32_16x16x32_bf16 v[68:71], v[208:211], v[192:195], v[68:71]
	s_setprio 1
	s_mov_b32 m0, s38
	v_lshl_add_u64 v[212:213], v[224:225], 0, s[60:61]
	s_barrier
	ds_read_b128 v[164:167], v150 offset:49152
	ds_read_b128 v[168:171], v150 offset:50176
	ds_read_b128 v[172:175], v150 offset:51200
	ds_read_b128 v[176:179], v150 offset:52224
	ds_read_b128 v[180:183], v150 offset:53248
	ds_read_b128 v[184:187], v150 offset:54272
	ds_read_b128 v[188:191], v150 offset:55296
	ds_read_b128 v[192:195], v150 offset:56320
	global_load_lds_dwordx4 v[212:213], off
	v_lshl_add_u64 v[212:213], v[230:231], 0, s[60:61]
	s_mov_b32 m0, s39
	s_nop 0
	global_load_lds_dwordx4 v[212:213], off
	s_barrier
	s_waitcnt lgkmcnt(0)
	s_setprio 0
	s_waitcnt lgkmcnt(0)
	v_mfma_f32_16x16x32_bf16 v[64:67], v[144:147], v[164:167], v[64:67]
	v_mfma_f32_16x16x32_bf16 v[60:63], v[156:159], v[164:167], v[60:63]
	v_mfma_f32_16x16x32_bf16 v[48:51], v[144:147], v[172:175], v[48:51]
	v_mfma_f32_16x16x32_bf16 v[44:47], v[156:159], v[172:175], v[44:47]
	v_mfma_f32_16x16x32_bf16 v[32:35], v[144:147], v[180:183], v[32:35]
	v_mfma_f32_16x16x32_bf16 v[28:31], v[156:159], v[180:183], v[28:31]
	v_mfma_f32_16x16x32_bf16 v[16:19], v[144:147], v[188:191], v[16:19]
	v_mfma_f32_16x16x32_bf16 v[12:15], v[156:159], v[188:191], v[12:15]
	v_mfma_f32_16x16x32_bf16 v[64:67], v[152:155], v[168:171], v[64:67]
	v_mfma_f32_16x16x32_bf16 v[60:63], v[160:163], v[168:171], v[60:63]
	v_mfma_f32_16x16x32_bf16 v[48:51], v[152:155], v[176:179], v[48:51]
	v_mfma_f32_16x16x32_bf16 v[44:47], v[160:163], v[176:179], v[44:47]
	v_mfma_f32_16x16x32_bf16 v[32:35], v[152:155], v[184:187], v[32:35]
	v_mfma_f32_16x16x32_bf16 v[28:31], v[160:163], v[184:187], v[28:31]
	v_mfma_f32_16x16x32_bf16 v[16:19], v[152:155], v[192:195], v[16:19]
	v_mfma_f32_16x16x32_bf16 v[12:15], v[160:163], v[192:195], v[12:15]
	s_setprio 1
	s_barrier
	s_add_u32 s16, s20, 0x40080
	s_addc_u32 s17, s21, 0
	s_add_i32 s20, s22, s29
	v_lshl_add_u64 v[144:145], s[16:17], 0, v[136:137]
	s_mov_b32 m0, s20
	s_nop 0
	global_load_lds_dwordx4 v[144:145], off
	v_lshl_add_u64 v[144:145], s[16:17], 0, v[132:133]
	s_add_i32 m0, s20, 0x2000
	s_nop 0
	global_load_lds_dwordx4 v[144:145], off
	s_waitcnt vmcnt(6)
	s_barrier
	s_setprio 0
	v_mfma_f32_16x16x32_bf16 v[56:59], v[196:199], v[164:167], v[56:59]
	v_mfma_f32_16x16x32_bf16 v[52:55], v[204:207], v[164:167], v[52:55]
	v_mfma_f32_16x16x32_bf16 v[40:43], v[196:199], v[172:175], v[40:43]
	v_mfma_f32_16x16x32_bf16 v[36:39], v[204:207], v[172:175], v[36:39]
	v_mfma_f32_16x16x32_bf16 v[24:27], v[196:199], v[180:183], v[24:27]
	v_mfma_f32_16x16x32_bf16 v[20:23], v[204:207], v[180:183], v[20:23]
	v_mfma_f32_16x16x32_bf16 v[8:11], v[196:199], v[188:191], v[8:11]
	v_mfma_f32_16x16x32_bf16 v[4:7], v[204:207], v[188:191], v[4:7]
	v_mfma_f32_16x16x32_bf16 v[56:59], v[200:203], v[168:171], v[56:59]
	v_mfma_f32_16x16x32_bf16 v[52:55], v[208:211], v[168:171], v[52:55]
	v_mfma_f32_16x16x32_bf16 v[40:43], v[200:203], v[176:179], v[40:43]
	v_mfma_f32_16x16x32_bf16 v[36:39], v[208:211], v[176:179], v[36:39]
	v_mfma_f32_16x16x32_bf16 v[24:27], v[200:203], v[184:187], v[24:27]
	v_mfma_f32_16x16x32_bf16 v[20:23], v[208:211], v[184:187], v[20:23]
	v_mfma_f32_16x16x32_bf16 v[8:11], v[200:203], v[192:195], v[8:11]
	v_mfma_f32_16x16x32_bf16 v[4:7], v[208:211], v[192:195], v[4:7]
	s_setprio 1
	s_add_i32 s45, s45, 2
	s_add_u32 s7, s7, 0x100
	s_addc_u32 s44, s44, 0
	s_cmp_gt_u32 s45, 13
	s_mov_b64 s[16:17], s[18:19]
	s_barrier
	s_cbranch_scc0 .LBB0_2136
	s_setprio 0
	v_mov_b32_e32 v2, v148
	s_lshl_b32 s7, s43, 8
	s_add_i32 s7, s7, s37
	v_and_b32_e32 v145, 64, v214
	v_bfe_u32 v153, v2, 4, 2
	v_and_or_b32 v144, v2, 15, s7
	v_xor_b32_e32 v2, 16, v214
	v_add_u32_e32 v145, 64, v145
	v_cmp_lt_i32_e32 vcc, v2, v145
	s_lshl_b32 s18, s42, 8
	s_ashr_i32 s19, s18, 31
	v_cndmask_b32_e32 v2, v214, v2, vcc
	v_lshlrev_b32_e32 v152, 2, v2
	v_xor_b32_e32 v2, 32, v214
	v_cmp_lt_i32_e32 vcc, v2, v145
	v_ashrrev_i32_e32 v145, 31, v144
	v_lshlrev_b64 v[146:147], 11, v[144:145]
	v_lshl_add_u64 v[146:147], s[4:5], 0, v[146:147]
	v_cndmask_b32_e32 v2, v214, v2, vcc
	v_lshl_add_u64 v[146:147], s[18:19], 1, v[146:147]
	v_lshlrev_b32_e32 v151, 2, v2
	v_lshl_add_u64 v[146:147], v[146:147], 0, s[50:51]
	v_lshlrev_b32_e32 v2, 4, v153
	v_lshl_add_u64 v[146:147], v[146:147], 0, v[2:3]
	global_load_dwordx4 v[160:163], v[146:147], off
	global_load_dwordx4 v[164:167], v[146:147], off offset:256
	s_mov_b32 s100, 0x8000
	s_mov_b32 s101, 0
	v_lshl_add_u64 v[210:211], v[146:147], 0, s[100:101]
	global_load_dwordx4 v[168:171], v[210:211], off
	global_load_dwordx4 v[172:175], v[210:211], off offset:256
	v_lshl_add_u64 v[210:211], v[210:211], 0, s[100:101]
	global_load_dwordx4 v[176:179], v[210:211], off
	global_load_dwordx4 v[180:183], v[210:211], off offset:256
	v_lshl_add_u64 v[210:211], v[210:211], 0, s[100:101]
	global_load_dwordx4 v[184:187], v[210:211], off
	global_load_dwordx4 v[188:191], v[210:211], off offset:256
	s_mov_b32 s100, 0x28000
	v_lshl_add_u64 v[210:211], v[210:211], 0, s[100:101]
	global_load_dwordx4 v[192:195], v[210:211], off
	global_load_dwordx4 v[198:201], v[210:211], off offset:256
	s_mov_b32 s100, 0x8000
	v_lshl_add_u64 v[210:211], v[210:211], 0, s[100:101]
	global_load_dwordx4 v[202:205], v[210:211], off
	global_load_dwordx4 v[206:209], v[210:211], off offset:256
	v_lshl_add_u64 v[210:211], v[210:211], 0, s[100:101]
	global_load_dwordx4 v[236:239], v[210:211], off
	global_load_dwordx4 v[240:243], v[210:211], off offset:256
	v_lshl_add_u64 v[210:211], v[210:211], 0, s[100:101]
	global_load_dwordx4 v[244:247], v[210:211], off
	global_load_dwordx4 v[248:251], v[210:211], off offset:256
	s_waitcnt vmcnt(0)
	v_mov_b32_e32 v154, v160
	v_mov_b32_e32 v155, v161
	v_mov_b32_e32 v156, v162
	v_mov_b32_e32 v157, v163
	s_lshl_b32 s16, s42, 2
	v_cmp_eq_u32_e32 vcc, 0, v153
	s_ashr_i32 s17, s16, 31
	v_lshlrev_b32_e32 v158, 16, v154
	v_and_b32_e32 v159, 0xffff0000, v154
	v_lshlrev_b32_e32 v154, 16, v155
	v_and_b32_e32 v155, 0xffff0000, v155
	v_pk_add_f32 v[130:131], v[130:131], v[154:155]
	v_lshlrev_b32_e32 v154, 16, v156
	v_and_b32_e32 v155, 0xffff0000, v156
	v_lshlrev_b32_e32 v156, 16, v157
	v_and_b32_e32 v157, 0xffff0000, v157
	v_pk_add_f32 v[128:129], v[128:129], v[158:159]
	v_pk_add_f32 v[156:157], v[126:127], v[156:157]
	v_pk_add_f32 v[154:155], v[124:125], v[154:155]
	v_cvt_pk_bf16_f32 v124, v128, v129
	v_cvt_pk_bf16_f32 v125, v130, v131
	v_cvt_pk_bf16_f32 v126, v154, v155
	v_cvt_pk_bf16_f32 v127, v156, v157
	global_store_dwordx4 v[146:147], v[124:127], off
	v_mul_f32_e32 v2, v129, v129
	v_fmac_f32_e32 v2, v128, v128
	v_mul_f32_e32 v124, v131, v131
	v_fmac_f32_e32 v124, v130, v130
	v_add_f32_e32 v2, v2, v124
	v_mul_f32_e32 v124, v155, v155
	v_fmac_f32_e32 v124, v154, v154
	v_add_f32_e32 v2, v124, v2
	v_mul_f32_e32 v124, v157, v157
	v_fmac_f32_e32 v124, v156, v156
	v_add_f32_e32 v2, v124, v2
	v_mov_b32_e32 v124, v164
	v_mov_b32_e32 v125, v165
	v_mov_b32_e32 v126, v166
	v_mov_b32_e32 v127, v167
	v_lshlrev_b32_e32 v128, 16, v124
	v_and_b32_e32 v129, 0xffff0000, v124
	v_lshlrev_b32_e32 v124, 16, v125
	v_and_b32_e32 v125, 0xffff0000, v125
	v_pk_add_f32 v[122:123], v[122:123], v[124:125]
	v_lshlrev_b32_e32 v124, 16, v126
	v_and_b32_e32 v125, 0xffff0000, v126
	v_lshlrev_b32_e32 v126, 16, v127
	v_and_b32_e32 v127, 0xffff0000, v127
	v_pk_add_f32 v[120:121], v[120:121], v[128:129]
	v_pk_add_f32 v[126:127], v[118:119], v[126:127]
	v_pk_add_f32 v[124:125], v[116:117], v[124:125]
	v_cvt_pk_bf16_f32 v116, v120, v121
	v_cvt_pk_bf16_f32 v117, v122, v123
	v_cvt_pk_bf16_f32 v118, v124, v125
	v_cvt_pk_bf16_f32 v119, v126, v127
	global_store_dwordx4 v[146:147], v[116:119], off offset:256
	s_nop 1
	v_mul_f32_e32 v116, v121, v121
	v_mul_f32_e32 v117, v123, v123
	v_fmac_f32_e32 v116, v120, v120
	v_fmac_f32_e32 v117, v122, v122
	v_add_f32_e32 v116, v116, v117
	v_mul_f32_e32 v117, v125, v125
	v_fmac_f32_e32 v117, v124, v124
	v_add_f32_e32 v116, v117, v116
	v_mul_f32_e32 v117, v127, v127
	v_fmac_f32_e32 v117, v126, v126
	v_add_f32_e32 v116, v117, v116
	v_add_f32_e32 v2, v2, v116
	ds_bpermute_b32 v116, v152, v2
	s_waitcnt lgkmcnt(0)
	v_add_f32_e32 v2, v2, v116
	ds_bpermute_b32 v116, v151, v2
	s_and_saveexec_b64 s[20:21], vcc
	s_cbranch_execz .LBB0_2139
	v_lshlrev_b64 v[118:119], 6, v[144:145]
	v_lshl_add_u64 v[118:119], s[2:3], 0, v[118:119]
	v_lshl_add_u64 v[118:119], s[16:17], 2, v[118:119]
	s_lshl_b32 s22, s36, 2
	s_mov_b32 s23, s51
	v_lshl_add_u64 v[118:119], v[118:119], 0, s[22:23]
	s_waitcnt lgkmcnt(0)
	v_add_f32_e32 v2, v2, v116
	global_store_dword v[118:119], v2, off

.LBB0_2367:
	s_setprio 0
	s_lshl_b32 s0, s43, 8
	v_mov_b32_e32 v137, v229
	s_and_b32 s2, s0, 0x100
	s_cmp_lt_i32 s21, 4
	v_and_or_b32 v134, v137, 15, s40
	s_cselect_b32 s50, 0, 0x400
	v_add_lshl_u32 v135, v134, s2, 2
	s_add_i32 s3, 0, 0x20900
	v_add_u32_e32 v2, s3, v135
	ds_read_b32 v2, v2
	s_add_i32 s4, 0, 0x21100
	v_add_u32_e32 v135, s4, v135
	ds_read_b32 v136, v135
	v_ashrrev_i32_e32 v135, 31, v134
	s_waitcnt lgkmcnt(0)
	v_pk_mul_f32 v[128:129], v[128:129], v[2:3] op_sel_hi:[1,0]
	v_lshlrev_b64 v[138:139], 11, v[134:135]
	v_mul_f32_e32 v135, 0xbfb8aa3b, v128
	v_exp_f32_e32 v135, v135
	v_pk_mul_f32 v[120:121], v[120:121], v[2:3] op_sel_hi:[1,0]
	v_pk_mul_f32 v[122:123], v[122:123], v[2:3] op_sel_hi:[1,0]
	v_pk_mul_f32 v[116:117], v[116:117], v[2:3] op_sel_hi:[1,0]
	v_add_f32_e32 v135, 1.0, v135
	v_rcp_f32_e32 v140, v135
	v_mul_f32_e32 v135, 0xbfb8aa3b, v129
	v_exp_f32_e32 v135, v135
	v_ashrrev_i32_e32 v191, 31, v190
	v_lshlrev_b64 v[132:133], 19, v[190:191]
	v_lshl_add_u64 v[132:133], s[16:17], 0, v[132:133]
	v_add_f32_e32 v135, 1.0, v135
	v_rcp_f32_e32 v141, v135
	v_lshl_add_u64 v[138:139], v[132:133], 0, v[138:139]
	s_lshl_b32 s0, s21, 8
	v_lshl_add_u64 v[138:139], v[138:139], 0, s[50:51]
	v_pk_mul_f32 v[128:129], v[128:129], v[140:141]
	s_and_b32 s0, s0, 0x300
	v_pk_mul_f32 v[120:121], v[120:121], v[128:129]
	v_pk_mul_f32 v[128:129], v[130:131], v[2:3] op_sel_hi:[1,0]
	v_pk_mul_f32 v[120:121], v[136:137], v[120:121] op_sel_hi:[0,1]
	v_mul_f32_e32 v130, 0xbfb8aa3b, v128
	v_mul_f32_e32 v131, 0xbfb8aa3b, v129
	v_exp_f32_e32 v130, v130
	v_exp_f32_e32 v131, v131
	v_cvt_pk_bf16_f32 v120, v120, v121
	s_mov_b32 s1, s51
	v_add_f32_e32 v130, 1.0, v130
	v_add_f32_e32 v131, 1.0, v131
	v_rcp_f32_e32 v130, v130
	v_rcp_f32_e32 v131, v131
	v_pk_mul_f32 v[118:119], v[118:119], v[2:3] op_sel_hi:[1,0]
	v_lshl_add_u64 v[138:139], v[138:139], 0, s[0:1]
	s_mov_b32 s21, s51
	v_pk_mul_f32 v[128:129], v[128:129], v[130:131]
	v_lshl_add_u64 v[138:139], v[138:139], 0, s[20:21]
	v_pk_mul_f32 v[122:123], v[122:123], v[128:129]
	s_and_b64 vcc, exec, s[6:7]
	v_pk_mul_f32 v[122:123], v[136:137], v[122:123] op_sel_hi:[0,1]
	v_cvt_pk_bf16_f32 v121, v122, v123
	v_pk_mul_f32 v[122:123], v[124:125], v[2:3] op_sel_hi:[1,0]
	v_mov_b32_e32 v192, v187
	v_mul_f32_e32 v124, 0xbfb8aa3b, v122
	v_mul_f32_e32 v125, 0xbfb8aa3b, v123
	v_exp_f32_e32 v124, v124
	v_exp_f32_e32 v125, v125
	v_mov_b32_e32 v196, v197
	v_mov_b32_e32 v194, v185
	v_add_f32_e32 v124, 1.0, v124
	v_add_f32_e32 v125, 1.0, v125
	v_rcp_f32_e32 v124, v124
	v_rcp_f32_e32 v125, v125
	v_mov_b32_e32 v198, v193
	v_mov_b32_e32 v190, v236
	s_mov_b32 s43, s42
	v_pk_mul_f32 v[122:123], v[122:123], v[124:125]
	s_nop 0
	v_pk_mul_f32 v[116:117], v[116:117], v[122:123]
	v_pk_mul_f32 v[122:123], v[126:127], v[2:3] op_sel_hi:[1,0]
	v_pk_mul_f32 v[116:117], v[136:137], v[116:117] op_sel_hi:[0,1]
	v_mul_f32_e32 v124, 0xbfb8aa3b, v122
	v_mul_f32_e32 v125, 0xbfb8aa3b, v123
	v_exp_f32_e32 v124, v124
	v_exp_f32_e32 v125, v125
	v_and_b32_e32 v2, 48, v137
	v_add_f32_e32 v124, 1.0, v124
	v_add_f32_e32 v125, 1.0, v125
	v_rcp_f32_e32 v124, v124
	v_rcp_f32_e32 v125, v125
	s_nop 0
	v_pk_mul_f32 v[122:123], v[122:123], v[124:125]
	s_nop 0
	v_pk_mul_f32 v[118:119], v[118:119], v[122:123]
	v_cvt_pk_bf16_f32 v122, v116, v117
	v_pk_mul_f32 v[118:119], v[136:137], v[118:119] op_sel_hi:[0,1]
	v_cvt_pk_bf16_f32 v123, v118, v119
	v_lshl_add_u64 v[116:117], v[138:139], 0, v[2:3]
	global_store_dwordx4 v[116:117], v[120:123], off
	v_or_b32_e32 v116, 16, v134
	v_add_lshl_u32 v117, v116, s2, 2
	v_add_u32_e32 v118, s3, v117
	ds_read_b32 v118, v118
	v_add_u32_e32 v117, s4, v117
	ds_read_b32 v120, v117
	v_ashrrev_i32_e32 v117, 31, v116
	v_lshlrev_b64 v[116:117], 11, v[116:117]
	s_waitcnt lgkmcnt(0)
	v_pk_mul_f32 v[112:113], v[112:113], v[118:119] op_sel_hi:[1,0]
	v_lshl_add_u64 v[116:117], v[132:133], 0, v[116:117]
	v_mul_f32_e32 v119, 0xbfb8aa3b, v112
	v_exp_f32_e32 v119, v119
	v_lshl_add_u64 v[116:117], v[116:117], 0, s[50:51]
	v_lshl_add_u64 v[116:117], v[116:117], 0, s[0:1]
	v_lshl_add_u64 v[116:117], v[116:117], 0, s[20:21]
	v_add_f32_e32 v119, 1.0, v119
	v_rcp_f32_e32 v122, v119
	v_mul_f32_e32 v119, 0xbfb8aa3b, v113
	v_exp_f32_e32 v119, v119
	s_nop 0
	v_add_f32_e32 v119, 1.0, v119
	v_rcp_f32_e32 v123, v119
	v_pk_mul_f32 v[104:105], v[104:105], v[118:119] op_sel_hi:[1,0]
	v_pk_mul_f32 v[106:107], v[106:107], v[118:119] op_sel_hi:[1,0]
	v_pk_mul_f32 v[100:101], v[100:101], v[118:119] op_sel_hi:[1,0]
	v_pk_mul_f32 v[112:113], v[112:113], v[122:123]
	v_pk_mul_f32 v[102:103], v[102:103], v[118:119] op_sel_hi:[1,0]
	v_pk_mul_f32 v[104:105], v[104:105], v[112:113]
	v_pk_mul_f32 v[112:113], v[114:115], v[118:119] op_sel_hi:[1,0]
	v_pk_mul_f32 v[104:105], v[120:121], v[104:105] op_sel_hi:[0,1]
	v_mul_f32_e32 v114, 0xbfb8aa3b, v112
	v_mul_f32_e32 v115, 0xbfb8aa3b, v113
	v_exp_f32_e32 v114, v114
	v_exp_f32_e32 v115, v115
	v_cvt_pk_bf16_f32 v104, v104, v105
	v_add_f32_e32 v114, 1.0, v114
	v_add_f32_e32 v115, 1.0, v115
	v_rcp_f32_e32 v114, v114
	v_rcp_f32_e32 v115, v115
	s_nop 0
	v_pk_mul_f32 v[112:113], v[112:113], v[114:115]
	s_nop 0
	v_pk_mul_f32 v[106:107], v[106:107], v[112:113]
	s_nop 0
	v_pk_mul_f32 v[106:107], v[120:121], v[106:107] op_sel_hi:[0,1]
	v_cvt_pk_bf16_f32 v105, v106, v107
	v_pk_mul_f32 v[106:107], v[108:109], v[118:119] op_sel_hi:[1,0]
	s_nop 0
	v_mul_f32_e32 v108, 0xbfb8aa3b, v106
	v_mul_f32_e32 v109, 0xbfb8aa3b, v107
	v_exp_f32_e32 v108, v108
	v_exp_f32_e32 v109, v109
	v_add_f32_e32 v108, 1.0, v108
	v_add_f32_e32 v109, 1.0, v109
	v_rcp_f32_e32 v108, v108
	v_rcp_f32_e32 v109, v109
	s_nop 0
	v_pk_mul_f32 v[106:107], v[106:107], v[108:109]
	s_nop 0
	v_pk_mul_f32 v[100:101], v[100:101], v[106:107]
	v_pk_mul_f32 v[106:107], v[110:111], v[118:119] op_sel_hi:[1,0]
	v_pk_mul_f32 v[100:101], v[120:121], v[100:101] op_sel_hi:[0,1]
	v_mul_f32_e32 v108, 0xbfb8aa3b, v106
	v_mul_f32_e32 v109, 0xbfb8aa3b, v107
	v_exp_f32_e32 v108, v108
	v_exp_f32_e32 v109, v109
	v_add_f32_e32 v108, 1.0, v108
	v_add_f32_e32 v109, 1.0, v109
	v_rcp_f32_e32 v108, v108
	v_rcp_f32_e32 v109, v109
	s_nop 0
	v_pk_mul_f32 v[106:107], v[106:107], v[108:109]
	s_nop 0
	v_pk_mul_f32 v[102:103], v[102:103], v[106:107]
	v_cvt_pk_bf16_f32 v106, v100, v101
	v_pk_mul_f32 v[102:103], v[120:121], v[102:103] op_sel_hi:[0,1]
	v_cvt_pk_bf16_f32 v107, v102, v103
	v_lshl_add_u64 v[100:101], v[116:117], 0, v[2:3]
	global_store_dwordx4 v[100:101], v[104:107], off
	v_or_b32_e32 v100, 32, v134
	v_add_lshl_u32 v101, v100, s2, 2
	v_add_u32_e32 v102, s3, v101
	ds_read_b32 v102, v102
	v_add_u32_e32 v101, s4, v101
	ds_read_b32 v104, v101
	v_ashrrev_i32_e32 v101, 31, v100
	v_lshlrev_b64 v[100:101], 11, v[100:101]
	s_waitcnt lgkmcnt(0)
	v_pk_mul_f32 v[96:97], v[96:97], v[102:103] op_sel_hi:[1,0]
	v_lshl_add_u64 v[100:101], v[132:133], 0, v[100:101]
	v_mul_f32_e32 v103, 0xbfb8aa3b, v96
	v_exp_f32_e32 v103, v103
	v_lshl_add_u64 v[100:101], v[100:101], 0, s[50:51]
	v_lshl_add_u64 v[100:101], v[100:101], 0, s[0:1]
	v_lshl_add_u64 v[100:101], v[100:101], 0, s[20:21]
	v_add_f32_e32 v103, 1.0, v103
	v_rcp_f32_e32 v106, v103
	v_mul_f32_e32 v103, 0xbfb8aa3b, v97
	v_exp_f32_e32 v103, v103
	s_nop 0
	v_add_f32_e32 v103, 1.0, v103
	v_rcp_f32_e32 v107, v103
	v_pk_mul_f32 v[88:89], v[88:89], v[102:103] op_sel_hi:[1,0]
	v_pk_mul_f32 v[90:91], v[90:91], v[102:103] op_sel_hi:[1,0]
	v_pk_mul_f32 v[84:85], v[84:85], v[102:103] op_sel_hi:[1,0]
	v_pk_mul_f32 v[96:97], v[96:97], v[106:107]
	v_pk_mul_f32 v[86:87], v[86:87], v[102:103] op_sel_hi:[1,0]
	v_pk_mul_f32 v[88:89], v[88:89], v[96:97]
	v_pk_mul_f32 v[96:97], v[98:99], v[102:103] op_sel_hi:[1,0]
	v_pk_mul_f32 v[88:89], v[104:105], v[88:89] op_sel_hi:[0,1]
	v_mul_f32_e32 v98, 0xbfb8aa3b, v96
	v_mul_f32_e32 v99, 0xbfb8aa3b, v97
	v_exp_f32_e32 v98, v98
	v_exp_f32_e32 v99, v99
	v_cvt_pk_bf16_f32 v88, v88, v89
	v_add_f32_e32 v98, 1.0, v98
	v_add_f32_e32 v99, 1.0, v99
	v_rcp_f32_e32 v98, v98
	v_rcp_f32_e32 v99, v99
	s_nop 0
	v_pk_mul_f32 v[96:97], v[96:97], v[98:99]
	s_nop 0
	v_pk_mul_f32 v[90:91], v[90:91], v[96:97]
	s_nop 0
	v_pk_mul_f32 v[90:91], v[104:105], v[90:91] op_sel_hi:[0,1]
	v_cvt_pk_bf16_f32 v89, v90, v91
	v_pk_mul_f32 v[90:91], v[92:93], v[102:103] op_sel_hi:[1,0]
	s_nop 0
	v_mul_f32_e32 v92, 0xbfb8aa3b, v90
	v_mul_f32_e32 v93, 0xbfb8aa3b, v91
	v_exp_f32_e32 v92, v92
	v_exp_f32_e32 v93, v93
	v_add_f32_e32 v92, 1.0, v92
	v_add_f32_e32 v93, 1.0, v93
	v_rcp_f32_e32 v92, v92
	v_rcp_f32_e32 v93, v93
	s_nop 0
	v_pk_mul_f32 v[90:91], v[90:91], v[92:93]
	s_nop 0
	v_pk_mul_f32 v[84:85], v[84:85], v[90:91]
	v_pk_mul_f32 v[90:91], v[94:95], v[102:103] op_sel_hi:[1,0]
	v_pk_mul_f32 v[84:85], v[104:105], v[84:85] op_sel_hi:[0,1]
	v_mul_f32_e32 v92, 0xbfb8aa3b, v90
	v_mul_f32_e32 v93, 0xbfb8aa3b, v91
	v_exp_f32_e32 v92, v92
	v_exp_f32_e32 v93, v93
	v_add_f32_e32 v92, 1.0, v92
	v_add_f32_e32 v93, 1.0, v93
	v_rcp_f32_e32 v92, v92
	v_rcp_f32_e32 v93, v93
	s_nop 0
	v_pk_mul_f32 v[90:91], v[90:91], v[92:93]
	s_nop 0
	v_pk_mul_f32 v[86:87], v[86:87], v[90:91]
	v_cvt_pk_bf16_f32 v90, v84, v85
	v_pk_mul_f32 v[86:87], v[104:105], v[86:87] op_sel_hi:[0,1]
	v_cvt_pk_bf16_f32 v91, v86, v87
	v_lshl_add_u64 v[84:85], v[100:101], 0, v[2:3]
	global_store_dwordx4 v[84:85], v[88:91], off
	s_nop 1
	v_or_b32_e32 v88, 48, v134
	v_add_lshl_u32 v85, v88, s2, 2
	v_add_u32_e32 v84, s3, v85
	ds_read_b32 v84, v84
	v_add_u32_e32 v85, s4, v85
	ds_read_b32 v86, v85
	v_ashrrev_i32_e32 v89, 31, v88
	v_lshlrev_b64 v[88:89], 11, v[88:89]
	s_waitcnt lgkmcnt(0)
	v_pk_mul_f32 v[80:81], v[80:81], v[84:85] op_sel_hi:[1,0]
	v_lshl_add_u64 v[88:89], v[132:133], 0, v[88:89]
	v_mul_f32_e32 v85, 0xbfb8aa3b, v80
	v_exp_f32_e32 v85, v85
	v_lshl_add_u64 v[88:89], v[88:89], 0, s[50:51]
	v_lshl_add_u64 v[88:89], v[88:89], 0, s[0:1]
	v_lshl_add_u64 v[88:89], v[88:89], 0, s[20:21]
	v_add_f32_e32 v85, 1.0, v85
	v_rcp_f32_e32 v90, v85
	v_mul_f32_e32 v85, 0xbfb8aa3b, v81
	v_exp_f32_e32 v85, v85
	s_nop 0
	v_add_f32_e32 v85, 1.0, v85
	v_rcp_f32_e32 v91, v85
	v_pk_mul_f32 v[72:73], v[72:73], v[84:85] op_sel_hi:[1,0]
	v_pk_mul_f32 v[74:75], v[74:75], v[84:85] op_sel_hi:[1,0]
	v_pk_mul_f32 v[68:69], v[68:69], v[84:85] op_sel_hi:[1,0]
	v_pk_mul_f32 v[80:81], v[80:81], v[90:91]
	v_pk_mul_f32 v[70:71], v[70:71], v[84:85] op_sel_hi:[1,0]
	v_pk_mul_f32 v[72:73], v[72:73], v[80:81]
	v_pk_mul_f32 v[80:81], v[82:83], v[84:85] op_sel_hi:[1,0]
	v_pk_mul_f32 v[72:73], v[86:87], v[72:73] op_sel_hi:[0,1]
	v_mul_f32_e32 v82, 0xbfb8aa3b, v80
	v_mul_f32_e32 v83, 0xbfb8aa3b, v81
	v_exp_f32_e32 v82, v82
	v_exp_f32_e32 v83, v83
	v_cvt_pk_bf16_f32 v72, v72, v73
	v_add_f32_e32 v82, 1.0, v82
	v_add_f32_e32 v83, 1.0, v83
	v_rcp_f32_e32 v82, v82
	v_rcp_f32_e32 v83, v83
	s_nop 0
	v_pk_mul_f32 v[80:81], v[80:81], v[82:83]
	s_nop 0
	v_pk_mul_f32 v[74:75], v[74:75], v[80:81]
	s_nop 0
	v_pk_mul_f32 v[74:75], v[86:87], v[74:75] op_sel_hi:[0,1]
	v_cvt_pk_bf16_f32 v73, v74, v75
	v_pk_mul_f32 v[74:75], v[76:77], v[84:85] op_sel_hi:[1,0]
	s_nop 0
	v_mul_f32_e32 v76, 0xbfb8aa3b, v74
	v_mul_f32_e32 v77, 0xbfb8aa3b, v75
	v_exp_f32_e32 v76, v76
	v_exp_f32_e32 v77, v77
	v_add_f32_e32 v76, 1.0, v76
	v_add_f32_e32 v77, 1.0, v77
	v_rcp_f32_e32 v76, v76
	v_rcp_f32_e32 v77, v77
	s_nop 0
	v_pk_mul_f32 v[74:75], v[74:75], v[76:77]
	s_nop 0
	v_pk_mul_f32 v[68:69], v[68:69], v[74:75]
	v_pk_mul_f32 v[74:75], v[78:79], v[84:85] op_sel_hi:[1,0]
	v_pk_mul_f32 v[68:69], v[86:87], v[68:69] op_sel_hi:[0,1]
	v_mul_f32_e32 v76, 0xbfb8aa3b, v74
	v_mul_f32_e32 v77, 0xbfb8aa3b, v75
	v_exp_f32_e32 v76, v76
	v_exp_f32_e32 v77, v77
	v_add_f32_e32 v76, 1.0, v76
	v_add_f32_e32 v77, 1.0, v77
	v_rcp_f32_e32 v76, v76
	v_rcp_f32_e32 v77, v77
	s_nop 0
	v_pk_mul_f32 v[74:75], v[74:75], v[76:77]
	s_nop 0
	v_pk_mul_f32 v[70:71], v[70:71], v[74:75]
	v_cvt_pk_bf16_f32 v74, v68, v69
	v_pk_mul_f32 v[70:71], v[86:87], v[70:71] op_sel_hi:[0,1]
	v_cvt_pk_bf16_f32 v75, v70, v71
	v_lshl_add_u64 v[68:69], v[88:89], 0, v[2:3]
	global_store_dwordx4 v[68:69], v[72:75], off
	v_add_u32_e32 v68, 0x80, v134
	v_add_lshl_u32 v69, v68, s2, 2
	v_add_u32_e32 v70, s3, v69
	ds_read_b32 v70, v70
	v_add_u32_e32 v69, s4, v69
	ds_read_b32 v72, v69
	v_ashrrev_i32_e32 v69, 31, v68
	v_lshlrev_b64 v[68:69], 11, v[68:69]
	s_waitcnt lgkmcnt(0)
	v_pk_mul_f32 v[64:65], v[64:65], v[70:71] op_sel_hi:[1,0]
	v_lshl_add_u64 v[68:69], v[132:133], 0, v[68:69]
	v_mul_f32_e32 v71, 0xbfb8aa3b, v64
	v_exp_f32_e32 v71, v71
	v_lshl_add_u64 v[68:69], v[68:69], 0, s[50:51]
	v_lshl_add_u64 v[68:69], v[68:69], 0, s[0:1]
	v_lshl_add_u64 v[68:69], v[68:69], 0, s[20:21]
	v_add_f32_e32 v71, 1.0, v71
	v_rcp_f32_e32 v74, v71
	v_mul_f32_e32 v71, 0xbfb8aa3b, v65
	v_exp_f32_e32 v71, v71
	s_nop 0
	v_add_f32_e32 v71, 1.0, v71
	v_rcp_f32_e32 v75, v71
	v_pk_mul_f32 v[56:57], v[56:57], v[70:71] op_sel_hi:[1,0]
	v_pk_mul_f32 v[58:59], v[58:59], v[70:71] op_sel_hi:[1,0]
	v_pk_mul_f32 v[52:53], v[52:53], v[70:71] op_sel_hi:[1,0]
	v_pk_mul_f32 v[64:65], v[64:65], v[74:75]
	v_pk_mul_f32 v[54:55], v[54:55], v[70:71] op_sel_hi:[1,0]
	v_pk_mul_f32 v[56:57], v[56:57], v[64:65]
	v_pk_mul_f32 v[64:65], v[66:67], v[70:71] op_sel_hi:[1,0]
	v_pk_mul_f32 v[56:57], v[72:73], v[56:57] op_sel_hi:[0,1]
	v_mul_f32_e32 v66, 0xbfb8aa3b, v64
	v_mul_f32_e32 v67, 0xbfb8aa3b, v65
	v_exp_f32_e32 v66, v66
	v_exp_f32_e32 v67, v67
	v_cvt_pk_bf16_f32 v56, v56, v57
	v_add_f32_e32 v66, 1.0, v66
	v_add_f32_e32 v67, 1.0, v67
	v_rcp_f32_e32 v66, v66
	v_rcp_f32_e32 v67, v67
	s_nop 0
	v_pk_mul_f32 v[64:65], v[64:65], v[66:67]
	s_nop 0
	v_pk_mul_f32 v[58:59], v[58:59], v[64:65]
	s_nop 0
	v_pk_mul_f32 v[58:59], v[72:73], v[58:59] op_sel_hi:[0,1]
	v_cvt_pk_bf16_f32 v57, v58, v59
	v_pk_mul_f32 v[58:59], v[60:61], v[70:71] op_sel_hi:[1,0]
	s_nop 0
	v_mul_f32_e32 v60, 0xbfb8aa3b, v58
	v_mul_f32_e32 v61, 0xbfb8aa3b, v59
	v_exp_f32_e32 v60, v60
	v_exp_f32_e32 v61, v61
	v_add_f32_e32 v60, 1.0, v60
	v_add_f32_e32 v61, 1.0, v61
	v_rcp_f32_e32 v60, v60
	v_rcp_f32_e32 v61, v61
	s_nop 0
	v_pk_mul_f32 v[58:59], v[58:59], v[60:61]
	s_nop 0
	v_pk_mul_f32 v[52:53], v[52:53], v[58:59]
	v_pk_mul_f32 v[58:59], v[62:63], v[70:71] op_sel_hi:[1,0]
	v_pk_mul_f32 v[52:53], v[72:73], v[52:53] op_sel_hi:[0,1]
	v_mul_f32_e32 v60, 0xbfb8aa3b, v58
	v_mul_f32_e32 v61, 0xbfb8aa3b, v59
	v_exp_f32_e32 v60, v60
	v_exp_f32_e32 v61, v61
	v_add_f32_e32 v60, 1.0, v60
	v_add_f32_e32 v61, 1.0, v61
	v_rcp_f32_e32 v60, v60
	v_rcp_f32_e32 v61, v61
	s_nop 0
	v_pk_mul_f32 v[58:59], v[58:59], v[60:61]
	s_nop 0
	v_pk_mul_f32 v[54:55], v[54:55], v[58:59]
	v_cvt_pk_bf16_f32 v58, v52, v53
	v_pk_mul_f32 v[54:55], v[72:73], v[54:55] op_sel_hi:[0,1]
	v_cvt_pk_bf16_f32 v59, v54, v55
	v_lshl_add_u64 v[52:53], v[68:69], 0, v[2:3]
	global_store_dwordx4 v[52:53], v[56:59], off
	v_add_u32_e32 v52, 0x90, v134
	v_add_lshl_u32 v53, v52, s2, 2
	v_add_u32_e32 v54, s3, v53
	ds_read_b32 v54, v54
	v_add_u32_e32 v53, s4, v53
	ds_read_b32 v56, v53
	v_ashrrev_i32_e32 v53, 31, v52
	v_lshlrev_b64 v[52:53], 11, v[52:53]
	s_waitcnt lgkmcnt(0)
	v_pk_mul_f32 v[48:49], v[48:49], v[54:55] op_sel_hi:[1,0]
	v_lshl_add_u64 v[52:53], v[132:133], 0, v[52:53]
	v_mul_f32_e32 v55, 0xbfb8aa3b, v48
	v_exp_f32_e32 v55, v55
	v_lshl_add_u64 v[52:53], v[52:53], 0, s[50:51]
	v_lshl_add_u64 v[52:53], v[52:53], 0, s[0:1]
	v_lshl_add_u64 v[52:53], v[52:53], 0, s[20:21]
	v_add_f32_e32 v55, 1.0, v55
	v_rcp_f32_e32 v58, v55
	v_mul_f32_e32 v55, 0xbfb8aa3b, v49
	v_exp_f32_e32 v55, v55
	s_nop 0
	v_add_f32_e32 v55, 1.0, v55
	v_rcp_f32_e32 v59, v55
	v_pk_mul_f32 v[40:41], v[40:41], v[54:55] op_sel_hi:[1,0]
	v_pk_mul_f32 v[42:43], v[42:43], v[54:55] op_sel_hi:[1,0]
	v_pk_mul_f32 v[36:37], v[36:37], v[54:55] op_sel_hi:[1,0]
	v_pk_mul_f32 v[48:49], v[48:49], v[58:59]
	v_pk_mul_f32 v[38:39], v[38:39], v[54:55] op_sel_hi:[1,0]
	v_pk_mul_f32 v[40:41], v[40:41], v[48:49]
	v_pk_mul_f32 v[48:49], v[50:51], v[54:55] op_sel_hi:[1,0]
	v_pk_mul_f32 v[40:41], v[56:57], v[40:41] op_sel_hi:[0,1]
	v_mul_f32_e32 v50, 0xbfb8aa3b, v48
	v_mul_f32_e32 v51, 0xbfb8aa3b, v49
	v_exp_f32_e32 v50, v50
	v_exp_f32_e32 v51, v51
	v_cvt_pk_bf16_f32 v40, v40, v41
	v_add_f32_e32 v50, 1.0, v50
	v_add_f32_e32 v51, 1.0, v51
	v_rcp_f32_e32 v50, v50
	v_rcp_f32_e32 v51, v51
	s_nop 0
	v_pk_mul_f32 v[48:49], v[48:49], v[50:51]
	s_nop 0
	v_pk_mul_f32 v[42:43], v[42:43], v[48:49]
	s_nop 0
	v_pk_mul_f32 v[42:43], v[56:57], v[42:43] op_sel_hi:[0,1]
	v_cvt_pk_bf16_f32 v41, v42, v43
	v_pk_mul_f32 v[42:43], v[44:45], v[54:55] op_sel_hi:[1,0]
	s_nop 0
	v_mul_f32_e32 v44, 0xbfb8aa3b, v42
	v_mul_f32_e32 v45, 0xbfb8aa3b, v43
	v_exp_f32_e32 v44, v44
	v_exp_f32_e32 v45, v45
	v_add_f32_e32 v44, 1.0, v44
	v_add_f32_e32 v45, 1.0, v45
	v_rcp_f32_e32 v44, v44
	v_rcp_f32_e32 v45, v45
	s_nop 0
	v_pk_mul_f32 v[42:43], v[42:43], v[44:45]
	s_nop 0
	v_pk_mul_f32 v[36:37], v[36:37], v[42:43]
	v_pk_mul_f32 v[42:43], v[46:47], v[54:55] op_sel_hi:[1,0]
	v_pk_mul_f32 v[36:37], v[56:57], v[36:37] op_sel_hi:[0,1]
	v_mul_f32_e32 v44, 0xbfb8aa3b, v42
	v_mul_f32_e32 v45, 0xbfb8aa3b, v43
	v_exp_f32_e32 v44, v44
	v_exp_f32_e32 v45, v45
	v_add_f32_e32 v44, 1.0, v44
	v_add_f32_e32 v45, 1.0, v45
	v_rcp_f32_e32 v44, v44
	v_rcp_f32_e32 v45, v45
	s_nop 0
	v_pk_mul_f32 v[42:43], v[42:43], v[44:45]
	s_nop 0
	v_pk_mul_f32 v[38:39], v[38:39], v[42:43]
	v_cvt_pk_bf16_f32 v42, v36, v37
	v_pk_mul_f32 v[38:39], v[56:57], v[38:39] op_sel_hi:[0,1]
	v_cvt_pk_bf16_f32 v43, v38, v39
	v_lshl_add_u64 v[36:37], v[52:53], 0, v[2:3]
	global_store_dwordx4 v[36:37], v[40:43], off
	v_add_u32_e32 v36, 0xa0, v134
	v_add_lshl_u32 v37, v36, s2, 2
	v_add_u32_e32 v38, s3, v37
	ds_read_b32 v38, v38
	v_add_u32_e32 v37, s4, v37
	ds_read_b32 v40, v37
	v_ashrrev_i32_e32 v37, 31, v36
	v_lshlrev_b64 v[36:37], 11, v[36:37]
	s_waitcnt lgkmcnt(0)
	v_pk_mul_f32 v[32:33], v[32:33], v[38:39] op_sel_hi:[1,0]
	v_lshl_add_u64 v[36:37], v[132:133], 0, v[36:37]
	v_mul_f32_e32 v39, 0xbfb8aa3b, v32
	v_exp_f32_e32 v39, v39
	v_lshl_add_u64 v[36:37], v[36:37], 0, s[50:51]
	v_lshl_add_u64 v[36:37], v[36:37], 0, s[0:1]
	v_lshl_add_u64 v[36:37], v[36:37], 0, s[20:21]
	v_add_f32_e32 v39, 1.0, v39
	v_rcp_f32_e32 v42, v39
	v_mul_f32_e32 v39, 0xbfb8aa3b, v33
	v_exp_f32_e32 v39, v39
	s_nop 0
	v_add_f32_e32 v39, 1.0, v39
	v_rcp_f32_e32 v43, v39
	v_pk_mul_f32 v[24:25], v[24:25], v[38:39] op_sel_hi:[1,0]
	v_pk_mul_f32 v[26:27], v[26:27], v[38:39] op_sel_hi:[1,0]
	v_pk_mul_f32 v[20:21], v[20:21], v[38:39] op_sel_hi:[1,0]
	v_pk_mul_f32 v[32:33], v[32:33], v[42:43]
	v_pk_mul_f32 v[22:23], v[22:23], v[38:39] op_sel_hi:[1,0]
	v_pk_mul_f32 v[24:25], v[24:25], v[32:33]
	v_pk_mul_f32 v[32:33], v[34:35], v[38:39] op_sel_hi:[1,0]
	v_pk_mul_f32 v[24:25], v[40:41], v[24:25] op_sel_hi:[0,1]
	v_mul_f32_e32 v34, 0xbfb8aa3b, v32
	v_mul_f32_e32 v35, 0xbfb8aa3b, v33
	v_exp_f32_e32 v34, v34
	v_exp_f32_e32 v35, v35
	v_cvt_pk_bf16_f32 v24, v24, v25
	v_add_f32_e32 v34, 1.0, v34
	v_add_f32_e32 v35, 1.0, v35
	v_rcp_f32_e32 v34, v34
	v_rcp_f32_e32 v35, v35
	s_nop 0
	v_pk_mul_f32 v[32:33], v[32:33], v[34:35]
	s_nop 0
	v_pk_mul_f32 v[26:27], v[26:27], v[32:33]
	s_nop 0
	v_pk_mul_f32 v[26:27], v[40:41], v[26:27] op_sel_hi:[0,1]
	v_cvt_pk_bf16_f32 v25, v26, v27
	v_pk_mul_f32 v[26:27], v[28:29], v[38:39] op_sel_hi:[1,0]
	s_nop 0
	v_mul_f32_e32 v28, 0xbfb8aa3b, v26
	v_mul_f32_e32 v29, 0xbfb8aa3b, v27
	v_exp_f32_e32 v28, v28
	v_exp_f32_e32 v29, v29
	v_add_f32_e32 v28, 1.0, v28
	v_add_f32_e32 v29, 1.0, v29
	v_rcp_f32_e32 v28, v28
	v_rcp_f32_e32 v29, v29
	s_nop 0
	v_pk_mul_f32 v[26:27], v[26:27], v[28:29]
	s_nop 0
	v_pk_mul_f32 v[20:21], v[20:21], v[26:27]
	v_pk_mul_f32 v[26:27], v[30:31], v[38:39] op_sel_hi:[1,0]
	v_pk_mul_f32 v[20:21], v[40:41], v[20:21] op_sel_hi:[0,1]
	v_mul_f32_e32 v28, 0xbfb8aa3b, v26
	v_mul_f32_e32 v29, 0xbfb8aa3b, v27
	v_exp_f32_e32 v28, v28
	v_exp_f32_e32 v29, v29
	v_add_f32_e32 v28, 1.0, v28
	v_add_f32_e32 v29, 1.0, v29
	v_rcp_f32_e32 v28, v28
	v_rcp_f32_e32 v29, v29
	s_nop 0
	v_pk_mul_f32 v[26:27], v[26:27], v[28:29]
	s_nop 0
	v_pk_mul_f32 v[22:23], v[22:23], v[26:27]
	v_cvt_pk_bf16_f32 v26, v20, v21
	v_pk_mul_f32 v[22:23], v[40:41], v[22:23] op_sel_hi:[0,1]
	v_cvt_pk_bf16_f32 v27, v22, v23
	v_lshl_add_u64 v[20:21], v[36:37], 0, v[2:3]
	global_store_dwordx4 v[20:21], v[24:27], off
	s_nop 1
	v_add_u32_e32 v24, 0xb0, v134
	v_add_lshl_u32 v21, v24, s2, 2
	v_add_u32_e32 v20, s3, v21
	ds_read_b32 v20, v20
	v_add_u32_e32 v21, s4, v21
	ds_read_b32 v22, v21
	v_ashrrev_i32_e32 v25, 31, v24
	v_lshlrev_b64 v[24:25], 11, v[24:25]
	s_waitcnt lgkmcnt(0)
	v_pk_mul_f32 v[16:17], v[16:17], v[20:21] op_sel_hi:[1,0]
	v_lshl_add_u64 v[24:25], v[132:133], 0, v[24:25]
	v_mul_f32_e32 v21, 0xbfb8aa3b, v16
	v_exp_f32_e32 v21, v21
	v_lshl_add_u64 v[24:25], v[24:25], 0, s[50:51]
	v_lshl_add_u64 v[24:25], v[24:25], 0, s[0:1]
	v_lshl_add_u64 v[24:25], v[24:25], 0, s[20:21]
	v_add_f32_e32 v21, 1.0, v21
	v_rcp_f32_e32 v26, v21
	v_mul_f32_e32 v21, 0xbfb8aa3b, v17
	v_exp_f32_e32 v21, v21
	s_mov_b32 s21, s41
	v_add_f32_e32 v21, 1.0, v21
	v_rcp_f32_e32 v27, v21
	v_pk_mul_f32 v[12:13], v[12:13], v[20:21] op_sel_hi:[1,0]
	v_pk_mul_f32 v[14:15], v[14:15], v[20:21] op_sel_hi:[1,0]
	v_pk_mul_f32 v[8:9], v[8:9], v[20:21] op_sel_hi:[1,0]
	v_pk_mul_f32 v[16:17], v[16:17], v[26:27]
	v_pk_mul_f32 v[4:5], v[4:5], v[20:21] op_sel_hi:[1,0]
	v_pk_mul_f32 v[12:13], v[12:13], v[16:17]
	v_pk_mul_f32 v[16:17], v[18:19], v[20:21] op_sel_hi:[1,0]
	v_pk_mul_f32 v[12:13], v[22:23], v[12:13] op_sel_hi:[0,1]
	v_mul_f32_e32 v18, 0xbfb8aa3b, v16
	v_mul_f32_e32 v19, 0xbfb8aa3b, v17
	v_exp_f32_e32 v18, v18
	v_exp_f32_e32 v19, v19
	v_cvt_pk_bf16_f32 v12, v12, v13
	v_pk_mul_f32 v[6:7], v[6:7], v[20:21] op_sel_hi:[1,0]
	v_add_f32_e32 v18, 1.0, v18
	v_add_f32_e32 v19, 1.0, v19
	v_rcp_f32_e32 v18, v18
	v_rcp_f32_e32 v19, v19
	s_nop 0
	v_pk_mul_f32 v[16:17], v[16:17], v[18:19]
	s_nop 0
	v_pk_mul_f32 v[14:15], v[14:15], v[16:17]
	s_nop 0
	v_pk_mul_f32 v[14:15], v[22:23], v[14:15] op_sel_hi:[0,1]
	v_cvt_pk_bf16_f32 v13, v14, v15
	v_mul_f32_e32 v14, 0xbfb8aa3b, v8
	v_mul_f32_e32 v15, 0xbfb8aa3b, v9
	v_exp_f32_e32 v14, v14
	v_exp_f32_e32 v15, v15
	v_add_f32_e32 v14, 1.0, v14
	v_add_f32_e32 v15, 1.0, v15
	v_rcp_f32_e32 v14, v14
	v_rcp_f32_e32 v15, v15
	s_nop 0
	v_pk_mul_f32 v[8:9], v[8:9], v[14:15]
	s_nop 0
	v_pk_mul_f32 v[4:5], v[4:5], v[8:9]
	v_pk_mul_f32 v[8:9], v[10:11], v[20:21] op_sel_hi:[1,0]
	v_pk_mul_f32 v[4:5], v[22:23], v[4:5] op_sel_hi:[0,1]
	v_mul_f32_e32 v10, 0xbfb8aa3b, v8
	v_mul_f32_e32 v11, 0xbfb8aa3b, v9
	v_exp_f32_e32 v10, v10
	v_exp_f32_e32 v11, v11
	v_cvt_pk_bf16_f32 v14, v4, v5
	v_lshl_add_u64 v[4:5], v[24:25], 0, v[2:3]
	v_add_f32_e32 v10, 1.0, v10
	v_add_f32_e32 v11, 1.0, v11
	v_rcp_f32_e32 v10, v10
	v_rcp_f32_e32 v11, v11
	s_nop 0
	v_pk_mul_f32 v[8:9], v[8:9], v[10:11]
	s_nop 0
	v_pk_mul_f32 v[6:7], v[6:7], v[8:9]
	s_nop 0
	v_pk_mul_f32 v[6:7], v[22:23], v[6:7] op_sel_hi:[0,1]
	v_cvt_pk_bf16_f32 v15, v6, v7
	global_store_dwordx4 v[4:5], v[12:15], off
	v_mov_b64_e32 v[4:5], v[188:189]
	s_cbranch_vccnz .LBB0_2378

.LBB0_2371:
	s_add_u32 s8, s12, s22
	s_addc_u32 s9, s13, s23
	s_add_u32 s26, s8, 0x100
	s_addc_u32 s27, s9, 0
	s_and_b64 s[8:9], s[4:5], exec
	v_lshl_add_u64 v[222:223], v[206:207], 0, s[22:23]
	s_cselect_b32 s9, s13, s27
	s_cselect_b32 s8, s12, s26
	v_cndmask_b32_e64 v251, v223, v191, s[4:5]
	v_cndmask_b32_e64 v250, v222, v239, s[4:5]
	s_barrier
	s_add_i32 s26, 0, 0x14000
	s_mov_b32 m0, s31
	v_add_u32_e32 v2, s26, v195
	v_lshl_add_u64 v[216:217], v[250:251], 0, v[180:181]
	ds_read_b128 v[242:245], v2
	ds_read_b128 v[246:249], v2 offset:1024
	ds_read_b128 v[222:225], v2 offset:2048
	ds_read_b128 v[230:233], v2 offset:3072
	global_load_lds_dwordx4 v[216:217], off
	v_lshl_add_u64 v[220:221], v[250:251], 0, v[182:183]
	s_mov_b32 m0, s34
	s_nop 0
	global_load_lds_dwordx4 v[220:221], off
	s_barrier
	s_waitcnt lgkmcnt(0)
	s_setprio 0
	s_waitcnt lgkmcnt(0)
	v_mfma_f32_16x16x32_bf16 v[120:123], v[242:245], v[172:175], v[120:123]
	v_mfma_f32_16x16x32_bf16 v[116:119], v[222:225], v[172:175], v[116:119]
	v_mfma_f32_16x16x32_bf16 v[104:107], v[242:245], v[164:167], v[104:107]
	v_mfma_f32_16x16x32_bf16 v[100:103], v[222:225], v[164:167], v[100:103]
	v_mfma_f32_16x16x32_bf16 v[88:91], v[242:245], v[156:159], v[88:91]
	v_mfma_f32_16x16x32_bf16 v[84:87], v[222:225], v[156:159], v[84:87]
	v_mfma_f32_16x16x32_bf16 v[72:75], v[242:245], v[148:151], v[72:75]
	v_mfma_f32_16x16x32_bf16 v[68:71], v[222:225], v[148:151], v[68:71]
	v_mfma_f32_16x16x32_bf16 v[120:123], v[246:249], v[176:179], v[120:123]
	v_mfma_f32_16x16x32_bf16 v[116:119], v[230:233], v[176:179], v[116:119]
	v_mfma_f32_16x16x32_bf16 v[104:107], v[246:249], v[168:171], v[104:107]
	v_mfma_f32_16x16x32_bf16 v[100:103], v[230:233], v[168:171], v[100:103]
	v_mfma_f32_16x16x32_bf16 v[88:91], v[246:249], v[160:163], v[88:91]
	v_mfma_f32_16x16x32_bf16 v[84:87], v[230:233], v[160:163], v[84:87]
	v_mfma_f32_16x16x32_bf16 v[72:75], v[246:249], v[152:155], v[72:75]
	v_mfma_f32_16x16x32_bf16 v[68:71], v[230:233], v[152:155], v[68:71]
	s_setprio 1
	s_mov_b32 m0, s30
	v_cndmask_b32_e64 v2, v194, v185, s[4:5]
	s_barrier
	ds_read_b128 v[148:151], v199 offset:16384
	ds_read_b128 v[152:155], v199 offset:17408
	ds_read_b128 v[156:159], v199 offset:18432
	ds_read_b128 v[160:163], v199 offset:19456
	ds_read_b128 v[164:167], v199 offset:20480
	ds_read_b128 v[168:171], v199 offset:21504
	ds_read_b128 v[172:175], v199 offset:22528
	ds_read_b128 v[176:179], v199 offset:23552
	v_cndmask_b32_e64 v208, v198, v193, s[4:5]
	global_load_lds_dwordx4 v2, s[8:9]
	s_mov_b32 m0, s35
	v_mov_b32_e32 v209, v3
	global_load_lds_dwordx4 v208, s[8:9]
	s_barrier
	s_waitcnt lgkmcnt(0)
	v_lshl_add_u64 v[210:211], s[8:9], 0, v[2:3]
	v_lshl_add_u64 v[208:209], s[8:9], 0, v[208:209]
	s_setprio 0
	s_waitcnt lgkmcnt(0)
	v_mfma_f32_16x16x32_bf16 v[64:67], v[132:135], v[148:151], v[64:67]
	v_mfma_f32_16x16x32_bf16 v[60:63], v[140:143], v[148:151], v[60:63]
	v_mfma_f32_16x16x32_bf16 v[48:51], v[132:135], v[156:159], v[48:51]
	v_mfma_f32_16x16x32_bf16 v[44:47], v[140:143], v[156:159], v[44:47]
	v_mfma_f32_16x16x32_bf16 v[32:35], v[132:135], v[164:167], v[32:35]
	v_mfma_f32_16x16x32_bf16 v[28:31], v[140:143], v[164:167], v[28:31]
	v_mfma_f32_16x16x32_bf16 v[16:19], v[132:135], v[172:175], v[16:19]
	v_mfma_f32_16x16x32_bf16 v[8:11], v[140:143], v[172:175], v[8:11]
	v_mfma_f32_16x16x32_bf16 v[64:67], v[136:139], v[152:155], v[64:67]
	v_mfma_f32_16x16x32_bf16 v[60:63], v[144:147], v[152:155], v[60:63]
	v_mfma_f32_16x16x32_bf16 v[48:51], v[136:139], v[160:163], v[48:51]
	v_mfma_f32_16x16x32_bf16 v[44:47], v[144:147], v[160:163], v[44:47]
	v_mfma_f32_16x16x32_bf16 v[32:35], v[136:139], v[168:171], v[32:35]
	v_mfma_f32_16x16x32_bf16 v[28:31], v[144:147], v[168:171], v[28:31]
	v_mfma_f32_16x16x32_bf16 v[16:19], v[136:139], v[176:179], v[16:19]
	v_mfma_f32_16x16x32_bf16 v[8:11], v[144:147], v[176:179], v[8:11]
	s_setprio 1
	s_barrier
	s_mov_b64 s[46:47], 0x40000
	v_lshl_add_u64 v[132:133], v[250:251], 0, s[46:47]
	s_add_i32 s26, s26, s29
	v_lshl_add_u64 v[134:135], v[132:133], 0, v[180:181]
	s_mov_b32 m0, s26
	v_lshl_add_u64 v[132:133], v[132:133], 0, v[182:183]
	global_load_lds_dwordx4 v[134:135], off
	s_add_i32 m0, s26, 0x2000
	s_nop 0
	global_load_lds_dwordx4 v[132:133], off
	s_waitcnt vmcnt(6)
	s_barrier
	s_setprio 0
	v_mfma_f32_16x16x32_bf16 v[56:59], v[242:245], v[148:151], v[56:59]
	v_mfma_f32_16x16x32_bf16 v[52:55], v[222:225], v[148:151], v[52:55]
	v_mfma_f32_16x16x32_bf16 v[40:43], v[242:245], v[156:159], v[40:43]
	v_mfma_f32_16x16x32_bf16 v[36:39], v[222:225], v[156:159], v[36:39]
	v_mfma_f32_16x16x32_bf16 v[24:27], v[242:245], v[164:167], v[24:27]
	v_mfma_f32_16x16x32_bf16 v[20:23], v[222:225], v[164:167], v[20:23]
	v_mfma_f32_16x16x32_bf16 v[12:15], v[242:245], v[172:175], v[12:15]
	v_mfma_f32_16x16x32_bf16 v[4:7], v[222:225], v[172:175], v[4:7]
	v_mfma_f32_16x16x32_bf16 v[56:59], v[246:249], v[152:155], v[56:59]
	v_mfma_f32_16x16x32_bf16 v[52:55], v[230:233], v[152:155], v[52:55]
	v_mfma_f32_16x16x32_bf16 v[40:43], v[246:249], v[160:163], v[40:43]
	v_mfma_f32_16x16x32_bf16 v[36:39], v[230:233], v[160:163], v[36:39]
	v_mfma_f32_16x16x32_bf16 v[24:27], v[246:249], v[168:171], v[24:27]
	v_mfma_f32_16x16x32_bf16 v[20:23], v[230:233], v[168:171], v[20:23]
	v_mfma_f32_16x16x32_bf16 v[12:15], v[246:249], v[176:179], v[12:15]
	v_mfma_f32_16x16x32_bf16 v[4:7], v[230:233], v[176:179], v[4:7]
	s_setprio 1
	s_add_i32 s26, 0, 0x18000
	v_add_u32_e32 v2, s26, v195
	s_barrier
	ds_read_b128 v[132:135], v2
	ds_read_b128 v[136:139], v2 offset:1024
	ds_read_b128 v[140:143], v2 offset:2048
	ds_read_b128 v[144:147], v2 offset:3072
	s_mov_b32 m0, s36
	v_cndmask_b32_e64 v2, v192, v187, s[4:5]
	ds_read_b128 v[148:151], v199 offset:32768
	ds_read_b128 v[152:155], v199 offset:33792
	ds_read_b128 v[156:159], v199 offset:34816
	ds_read_b128 v[160:163], v199 offset:35840
	ds_read_b128 v[164:167], v199 offset:36864
	ds_read_b128 v[168:171], v199 offset:37888
	ds_read_b128 v[172:175], v199 offset:38912
	ds_read_b128 v[176:179], v199 offset:39936
	v_cndmask_b32_e64 v222, v196, v197, s[4:5]
	global_load_lds_dwordx4 v2, s[8:9]
	s_mov_b32 m0, s37
	s_nop 0
	global_load_lds_dwordx4 v222, s[8:9]
	s_waitcnt lgkmcnt(8)
	s_barrier
	s_waitcnt lgkmcnt(0)
	s_setprio 0
	s_waitcnt lgkmcnt(0)
	v_mfma_f32_16x16x32_bf16 v[128:131], v[132:135], v[148:151], v[128:131]
	v_mfma_f32_16x16x32_bf16 v[124:127], v[140:143], v[148:151], v[124:127]
	v_mfma_f32_16x16x32_bf16 v[112:115], v[132:135], v[156:159], v[112:115]
	v_mfma_f32_16x16x32_bf16 v[108:111], v[140:143], v[156:159], v[108:111]
	v_mfma_f32_16x16x32_bf16 v[96:99], v[132:135], v[164:167], v[96:99]
	v_mfma_f32_16x16x32_bf16 v[92:95], v[140:143], v[164:167], v[92:95]
	v_mfma_f32_16x16x32_bf16 v[80:83], v[132:135], v[172:175], v[80:83]
	v_mfma_f32_16x16x32_bf16 v[76:79], v[140:143], v[172:175], v[76:79]
	v_mfma_f32_16x16x32_bf16 v[128:131], v[136:139], v[152:155], v[128:131]
	v_mfma_f32_16x16x32_bf16 v[124:127], v[144:147], v[152:155], v[124:127]
	v_mfma_f32_16x16x32_bf16 v[112:115], v[136:139], v[160:163], v[112:115]
	v_mfma_f32_16x16x32_bf16 v[108:111], v[144:147], v[160:163], v[108:111]
	v_mfma_f32_16x16x32_bf16 v[96:99], v[136:139], v[168:171], v[96:99]
	v_mfma_f32_16x16x32_bf16 v[92:95], v[144:147], v[168:171], v[92:95]
	v_mfma_f32_16x16x32_bf16 v[80:83], v[136:139], v[176:179], v[80:83]
	v_mfma_f32_16x16x32_bf16 v[76:79], v[144:147], v[176:179], v[76:79]
	s_setprio 1
	s_barrier
	s_add_i32 s4, 0, 0x1c000
	s_add_i32 s5, s26, s29
	v_add_u32_e32 v2, s4, v195
	v_lshl_add_u64 v[216:217], v[216:217], 0, s[60:61]
	s_mov_b32 m0, s5
	ds_read_b128 v[222:225], v2
	ds_read_b128 v[230:233], v2 offset:1024
	ds_read_b128 v[242:245], v2 offset:2048
	ds_read_b128 v[246:249], v2 offset:3072
	global_load_lds_dwordx4 v[216:217], off
	v_lshl_add_u64 v[216:217], v[220:221], 0, s[60:61]
	s_add_i32 m0, s5, 0x2000
	s_nop 0
	global_load_lds_dwordx4 v[216:217], off
	s_barrier
	s_waitcnt lgkmcnt(0)
	s_setprio 0
	s_waitcnt lgkmcnt(0)
	v_mfma_f32_16x16x32_bf16 v[120:123], v[222:225], v[148:151], v[120:123]
	v_mfma_f32_16x16x32_bf16 v[116:119], v[242:245], v[148:151], v[116:119]
	v_mfma_f32_16x16x32_bf16 v[104:107], v[222:225], v[156:159], v[104:107]
	v_mfma_f32_16x16x32_bf16 v[100:103], v[242:245], v[156:159], v[100:103]
	v_mfma_f32_16x16x32_bf16 v[88:91], v[222:225], v[164:167], v[88:91]
	v_mfma_f32_16x16x32_bf16 v[84:87], v[242:245], v[164:167], v[84:87]
	v_mfma_f32_16x16x32_bf16 v[72:75], v[222:225], v[172:175], v[72:75]
	v_mfma_f32_16x16x32_bf16 v[68:71], v[242:245], v[172:175], v[68:71]
	v_mfma_f32_16x16x32_bf16 v[120:123], v[230:233], v[152:155], v[120:123]
	v_mfma_f32_16x16x32_bf16 v[116:119], v[246:249], v[152:155], v[116:119]
	v_mfma_f32_16x16x32_bf16 v[104:107], v[230:233], v[160:163], v[104:107]
	v_mfma_f32_16x16x32_bf16 v[100:103], v[246:249], v[160:163], v[100:103]
	v_mfma_f32_16x16x32_bf16 v[88:91], v[230:233], v[168:171], v[88:91]
	v_mfma_f32_16x16x32_bf16 v[84:87], v[246:249], v[168:171], v[84:87]
	v_mfma_f32_16x16x32_bf16 v[72:75], v[230:233], v[176:179], v[72:75]
	v_mfma_f32_16x16x32_bf16 v[68:71], v[246:249], v[176:179], v[68:71]
	s_setprio 1
	s_mov_b32 m0, s38
	v_lshl_add_u64 v[210:211], v[210:211], 0, s[60:61]
	s_barrier
	ds_read_b128 v[148:151], v199 offset:49152
	ds_read_b128 v[152:155], v199 offset:50176
	ds_read_b128 v[156:159], v199 offset:51200
	ds_read_b128 v[160:163], v199 offset:52224
	ds_read_b128 v[164:167], v199 offset:53248
	ds_read_b128 v[168:171], v199 offset:54272
	ds_read_b128 v[172:175], v199 offset:55296
	ds_read_b128 v[176:179], v199 offset:56320
	global_load_lds_dwordx4 v[210:211], off
	v_lshl_add_u64 v[208:209], v[208:209], 0, s[60:61]
	s_mov_b32 m0, s39
	s_nop 0
	global_load_lds_dwordx4 v[208:209], off
	s_barrier
	s_waitcnt lgkmcnt(0)
	s_setprio 0
	s_waitcnt lgkmcnt(0)
	v_mfma_f32_16x16x32_bf16 v[64:67], v[132:135], v[148:151], v[64:67]
	v_mfma_f32_16x16x32_bf16 v[60:63], v[140:143], v[148:151], v[60:63]
	v_mfma_f32_16x16x32_bf16 v[48:51], v[132:135], v[156:159], v[48:51]
	v_mfma_f32_16x16x32_bf16 v[44:47], v[140:143], v[156:159], v[44:47]
	v_mfma_f32_16x16x32_bf16 v[32:35], v[132:135], v[164:167], v[32:35]
	v_mfma_f32_16x16x32_bf16 v[28:31], v[140:143], v[164:167], v[28:31]
	v_mfma_f32_16x16x32_bf16 v[16:19], v[132:135], v[172:175], v[16:19]
	v_mfma_f32_16x16x32_bf16 v[8:11], v[140:143], v[172:175], v[8:11]
	v_mfma_f32_16x16x32_bf16 v[64:67], v[136:139], v[152:155], v[64:67]
	v_mfma_f32_16x16x32_bf16 v[60:63], v[144:147], v[152:155], v[60:63]
	v_mfma_f32_16x16x32_bf16 v[48:51], v[136:139], v[160:163], v[48:51]
	v_mfma_f32_16x16x32_bf16 v[44:47], v[144:147], v[160:163], v[44:47]
	v_mfma_f32_16x16x32_bf16 v[32:35], v[136:139], v[168:171], v[32:35]
	v_mfma_f32_16x16x32_bf16 v[28:31], v[144:147], v[168:171], v[28:31]
	v_mfma_f32_16x16x32_bf16 v[16:19], v[136:139], v[176:179], v[16:19]
	v_mfma_f32_16x16x32_bf16 v[8:11], v[144:147], v[176:179], v[8:11]
	s_setprio 1
	s_barrier
	s_mov_b64 s[8:9], 0x40080
	v_lshl_add_u64 v[132:133], v[250:251], 0, s[8:9]
	s_add_i32 s4, s4, s29
	v_lshl_add_u64 v[134:135], v[132:133], 0, v[180:181]
	s_mov_b32 m0, s4
	v_lshl_add_u64 v[132:133], v[132:133], 0, v[182:183]
	global_load_lds_dwordx4 v[134:135], off
	s_add_i32 m0, s4, 0x2000
	s_nop 0
	global_load_lds_dwordx4 v[132:133], off
	s_waitcnt vmcnt(6)
	s_barrier
	s_setprio 0
	v_mfma_f32_16x16x32_bf16 v[56:59], v[222:225], v[148:151], v[56:59]
	v_mfma_f32_16x16x32_bf16 v[52:55], v[242:245], v[148:151], v[52:55]
	v_mfma_f32_16x16x32_bf16 v[40:43], v[222:225], v[156:159], v[40:43]
	v_mfma_f32_16x16x32_bf16 v[36:39], v[242:245], v[156:159], v[36:39]
	v_mfma_f32_16x16x32_bf16 v[24:27], v[222:225], v[164:167], v[24:27]
	v_mfma_f32_16x16x32_bf16 v[20:23], v[242:245], v[164:167], v[20:23]
	v_mfma_f32_16x16x32_bf16 v[12:15], v[222:225], v[172:175], v[12:15]
	v_mfma_f32_16x16x32_bf16 v[4:7], v[242:245], v[172:175], v[4:7]
	v_mfma_f32_16x16x32_bf16 v[56:59], v[230:233], v[152:155], v[56:59]
	v_mfma_f32_16x16x32_bf16 v[52:55], v[246:249], v[152:155], v[52:55]
	v_mfma_f32_16x16x32_bf16 v[40:43], v[230:233], v[160:163], v[40:43]
	v_mfma_f32_16x16x32_bf16 v[36:39], v[246:249], v[160:163], v[36:39]
	v_mfma_f32_16x16x32_bf16 v[24:27], v[230:233], v[168:171], v[24:27]
	v_mfma_f32_16x16x32_bf16 v[20:23], v[246:249], v[168:171], v[20:23]
	v_mfma_f32_16x16x32_bf16 v[12:15], v[230:233], v[176:179], v[12:15]
	v_mfma_f32_16x16x32_bf16 v[4:7], v[246:249], v[176:179], v[4:7]
	s_setprio 1
	s_add_i32 s45, s45, 2
	s_add_u32 s22, s22, 0x100
	s_addc_u32 s23, s23, 0
	s_cmp_gt_u32 s45, 13
	s_barrier
	s_cbranch_scc1 .LBB0_2367

.LBB0_2376:
	v_add_u32_e32 v2, 0, v195
	v_add_u32_e32 v2, 0x10000, v2
	ds_read_b128 v[132:135], v2
	ds_read_b128 v[136:139], v2 offset:1024
	ds_read_b128 v[140:143], v2 offset:2048
	ds_read_b128 v[144:147], v2 offset:3072
	v_lshl_add_u64 v[222:223], v[204:205], 0, s[22:23]
	s_add_i32 m0, s30, 0xc000
	ds_read_b128 v[172:175], v199
	ds_read_b128 v[176:179], v199 offset:1024
	ds_read_b128 v[164:167], v199 offset:2048
	ds_read_b128 v[168:171], v199 offset:3072
	ds_read_b128 v[156:159], v199 offset:4096
	ds_read_b128 v[160:163], v199 offset:5120
	ds_read_b128 v[148:151], v199 offset:6144
	ds_read_b128 v[152:155], v199 offset:7168
	global_load_lds_dwordx4 v[222:223], off
	v_lshl_add_u64 v[222:223], v[202:203], 0, s[22:23]
	s_add_i32 m0, s30, 0xe000
	s_nop 0
	global_load_lds_dwordx4 v[222:223], off
	s_waitcnt lgkmcnt(8)
	s_barrier
	s_waitcnt lgkmcnt(0)
	s_setprio 0
	s_waitcnt lgkmcnt(0)
	v_mfma_f32_16x16x32_bf16 v[128:131], v[132:135], v[172:175], v[128:131]
	v_mfma_f32_16x16x32_bf16 v[124:127], v[140:143], v[172:175], v[124:127]
	v_mfma_f32_16x16x32_bf16 v[112:115], v[132:135], v[164:167], v[112:115]
	v_mfma_f32_16x16x32_bf16 v[108:111], v[140:143], v[164:167], v[108:111]
	v_mfma_f32_16x16x32_bf16 v[96:99], v[132:135], v[156:159], v[96:99]
	v_mfma_f32_16x16x32_bf16 v[92:95], v[140:143], v[156:159], v[92:95]
	v_mfma_f32_16x16x32_bf16 v[80:83], v[132:135], v[148:151], v[80:83]
	v_mfma_f32_16x16x32_bf16 v[76:79], v[140:143], v[148:151], v[76:79]
	v_mfma_f32_16x16x32_bf16 v[128:131], v[136:139], v[176:179], v[128:131]
	v_mfma_f32_16x16x32_bf16 v[124:127], v[144:147], v[176:179], v[124:127]
	v_mfma_f32_16x16x32_bf16 v[112:115], v[136:139], v[168:171], v[112:115]
	v_mfma_f32_16x16x32_bf16 v[108:111], v[144:147], v[168:171], v[108:111]
	v_mfma_f32_16x16x32_bf16 v[96:99], v[136:139], v[160:163], v[96:99]
	v_mfma_f32_16x16x32_bf16 v[92:95], v[144:147], v[160:163], v[92:95]
	v_mfma_f32_16x16x32_bf16 v[80:83], v[136:139], v[152:155], v[80:83]
	v_mfma_f32_16x16x32_bf16 v[76:79], v[144:147], v[152:155], v[76:79]
	s_setprio 1
	s_and_b64 vcc, exec, s[8:9]
	s_cbranch_vccnz .LBB0_2371
	ds_read2st64_b32 v[222:223], v240 offset1:2
	s_waitcnt lgkmcnt(0)
	v_max_i32_e32 v2, 0, v222
	v_lshl_add_u32 v185, v2, 11, v212
	v_max_i32_e32 v2, 0, v223
	ds_read2st64_b32 v[222:223], v241 offset1:2
	v_lshl_add_u32 v187, v2, 11, v212
	s_waitcnt lgkmcnt(0)
	v_max_i32_e32 v2, 0, v222
	v_lshl_add_u32 v193, v2, 11, v235
	v_max_i32_e32 v2, 0, v223
	v_lshl_add_u32 v197, v2, 11, v235
	s_branch .LBB0_2371
